# s17
# baseline (speedup 1.0000x reference)
.LBB0_18:
	s_or_b64 exec, exec, s[6:7]
	s_waitcnt vmcnt(22)
	v_cmp_eq_u32_e32 vcc, 22, v106
	v_cvt_f16_f32_e32 v89, v117
	v_cvt_f16_f32_e32 v88, v116
	v_cvt_f16_f32_e32 v90, v113
	v_cndmask_b32_e64 v88, 0, v88, s[2:3]
	v_cndmask_b32_e32 v89, 0, v89, vcc
	v_cndmask_b32_e64 v89, v89, v90, s[4:5]
	v_pack_b32_f16 v96, v88, v89
	global_store_dword v123, v96, s[32:33]
	s_waitcnt vmcnt(21)
	v_cvt_pk_f16_f32 v66, v66, v70
	v_cvt_pk_f16_f32 v67, v67, v71
	v_cvt_pk_f16_f32 v68, v68, v72
	v_cvt_pk_f16_f32 v69, v69, v73
	ds_write2_b32 v136, v66, v67 offset0:0 offset1:68
	ds_write2_b32 v136, v68, v69 offset0:136 offset1:204
	s_waitcnt vmcnt(19)
	v_cvt_pk_f16_f32 v74, v74, v78
	v_cvt_pk_f16_f32 v75, v75, v79
	v_cvt_pk_f16_f32 v76, v76, v80
	v_cvt_pk_f16_f32 v77, v77, v81
	ds_write2_b32 v136, v74, v75 offset0:32 offset1:100
	ds_write2_b32 v136, v76, v77 offset0:168 offset1:236
	s_waitcnt vmcnt(17)
	v_cvt_pk_f16_f32 v58, v58, v62
	v_cvt_pk_f16_f32 v59, v59, v63
	v_cvt_pk_f16_f32 v60, v60, v64
	v_cvt_pk_f16_f32 v61, v61, v65
	ds_write2_b32 v137, v58, v59 offset0:0 offset1:68
	ds_write2_b32 v137, v60, v61 offset0:136 offset1:204
	s_waitcnt vmcnt(15)
	v_cvt_pk_f16_f32 v50, v50, v54
	v_cvt_pk_f16_f32 v51, v51, v55
	v_cvt_pk_f16_f32 v52, v52, v56
	v_cvt_pk_f16_f32 v53, v53, v57
	ds_write2_b32 v137, v50, v51 offset0:32 offset1:100
	ds_write2_b32 v137, v52, v53 offset0:168 offset1:236
	s_waitcnt vmcnt(13)
	v_cvt_pk_f16_f32 v42, v42, v46
	v_cvt_pk_f16_f32 v43, v43, v47
	v_cvt_pk_f16_f32 v44, v44, v48
	v_cvt_pk_f16_f32 v45, v45, v49
	ds_write2_b32 v138, v42, v43 offset0:0 offset1:68
	ds_write2_b32 v138, v44, v45 offset0:136 offset1:204
	s_waitcnt vmcnt(11)
	v_cvt_pk_f16_f32 v34, v34, v38
	v_cvt_pk_f16_f32 v35, v35, v39
	v_cvt_pk_f16_f32 v36, v36, v40
	v_cvt_pk_f16_f32 v37, v37, v41
	ds_write2_b32 v138, v34, v35 offset0:32 offset1:100
	ds_write2_b32 v138, v36, v37 offset0:168 offset1:236
	s_movk_i32 s0, 0x110
	v_lshlrev_b32_e32 v48, 4, v110
	v_mad_u32_u24 v48, v1, s0, v48
	s_waitcnt lgkmcnt(0)
	s_barrier
	ds_read_b128 v[144:147], v48
	ds_read_b128 v[152:155], v48 offset:4352
	ds_read_b128 v[160:163], v48 offset:8704
	ds_read_b128 v[148:151], v48 offset:64
	ds_read_b128 v[156:159], v48 offset:4416
	ds_read_b128 v[164:167], v48 offset:8768
	ds_read_b128 v[168:171], v48 offset:128
	ds_read_b128 v[176:179], v48 offset:4480
	ds_read_b128 v[184:187], v48 offset:8832
	ds_read_b128 v[172:175], v48 offset:192
	ds_read_b128 v[180:183], v48 offset:4544
	ds_read_b128 v[188:191], v48 offset:8896
	s_waitcnt vmcnt(9)
	v_cvt_pk_f16_f32 v39, v32, v33
	v_cvt_pk_f16_f32 v38, v30, v31
	v_cvt_pk_f16_f32 v37, v28, v29
	v_cvt_pk_f16_f32 v36, v26, v27
	s_waitcnt lgkmcnt(9)
	s_nop 0
	v_mfma_f32_16x16x32_f16 v[124:127], v[144:147], v[36:39], 0
	v_mfma_f32_16x16x32_f16 v[128:131], v[152:155], v[36:39], 0
	v_mfma_f32_16x16x32_f16 v[132:135], v[36:39], v[160:163], 0
	s_waitcnt vmcnt(7)
	v_cvt_pk_f16_f32 v25, v24, v25
	v_cvt_pk_f16_f32 v24, v22, v23
	v_cvt_pk_f16_f32 v23, v20, v21
	v_cvt_pk_f16_f32 v22, v18, v19
	s_waitcnt lgkmcnt(6)
	s_nop 0
	v_mfma_f32_16x16x32_f16 v[124:127], v[148:151], v[22:25], v[124:127]
	v_mfma_f32_16x16x32_f16 v[128:131], v[156:159], v[22:25], v[128:131]
	v_mfma_f32_16x16x32_f16 v[132:135], v[22:25], v[164:167], v[132:135]
	s_waitcnt vmcnt(5)
	v_cvt_pk_f16_f32 v43, v16, v17
	v_cvt_pk_f16_f32 v42, v14, v15
	v_cvt_pk_f16_f32 v41, v12, v13
	v_cvt_pk_f16_f32 v40, v10, v11
	s_waitcnt lgkmcnt(3)
	s_nop 0
	v_mfma_f32_16x16x32_f16 v[124:127], v[168:171], v[40:43], v[124:127]
	v_mfma_f32_16x16x32_f16 v[128:131], v[176:179], v[40:43], v[128:131]
	v_mfma_f32_16x16x32_f16 v[132:135], v[40:43], v[184:187], v[132:135]
	s_waitcnt vmcnt(3)
	v_cvt_pk_f16_f32 v9, v8, v9
	v_cvt_pk_f16_f32 v8, v6, v7
	v_cvt_pk_f16_f32 v7, v4, v5
	v_cvt_pk_f16_f32 v6, v2, v3
	s_waitcnt lgkmcnt(0)
	s_nop 0
	v_mfma_f32_16x16x32_f16 v[124:127], v[172:175], v[6:9], v[124:127]
	v_mfma_f32_16x16x32_f16 v[128:131], v[180:183], v[6:9], v[128:131]
	v_mfma_f32_16x16x32_f16 v[132:135], v[6:9], v[188:191], v[132:135]
	s_nop 5
	v_mul_f32_e32 v96, 0x403504f3, v124
	v_mul_f32_e32 v97, 0x403504f3, v125
	v_mul_f32_e32 v98, 0x403504f3, v126
	v_mul_f32_e32 v99, 0x403504f3, v127
	v_cvt_pk_fp8_f32 v100, v96, v97
	v_cvt_pk_fp8_f32 v100, v98, v99 op_sel:[0,0,1]
	v_mul_f32_e32 v96, 4.0, v128
	v_mul_f32_e32 v97, 4.0, v129
	v_mul_f32_e32 v98, 4.0, v130
	v_mul_f32_e32 v99, 4.0, v131
	v_cvt_pk_fp8_f32 v101, v96, v97
	v_cvt_pk_fp8_f32 v101, v98, v99 op_sel:[0,0,1]
	global_store_dword v140, v100, s[32:33]
	global_store_dword v139, v101, s[32:33]
	v_mul_f32_e32 v96, 4.0, v132
	v_mul_f32_e32 v97, 4.0, v133
	v_mul_f32_e32 v98, 4.0, v134
	v_mul_f32_e32 v99, 4.0, v135
	v_cvt_pk_fp8_f32 v102, v96, v97
	v_cvt_pk_fp8_f32 v102, v98, v99 op_sel:[0,0,1]
	s_nop 0
	global_store_dword v122, v102, s[32:33]
	s_endpgm

	.amdhsa_kernel _Z11prep_kernelPKfS0_PKiS2_S0_S0_S0_S0_S0_S0_Pc
		.amdhsa_group_segment_fixed_size 13056
		.amdhsa_private_segment_fixed_size 0
		.amdhsa_kernarg_size 88
		.amdhsa_user_sgpr_count 2
		.amdhsa_user_sgpr_dispatch_ptr 0
		.amdhsa_user_sgpr_queue_ptr 0
		.amdhsa_user_sgpr_kernarg_segment_ptr 1
		.amdhsa_user_sgpr_dispatch_id 0
		.amdhsa_user_sgpr_kernarg_preload_length 0
		.amdhsa_user_sgpr_kernarg_preload_offset 0
		.amdhsa_user_sgpr_private_segment_size 0
		.amdhsa_uses_dynamic_stack 0
		.amdhsa_enable_private_segment 0
		.amdhsa_system_sgpr_workgroup_id_x 1
		.amdhsa_system_sgpr_workgroup_id_y 0
		.amdhsa_system_sgpr_workgroup_id_z 0
		.amdhsa_system_sgpr_workgroup_info 0
		.amdhsa_system_vgpr_workitem_id 0
		.amdhsa_next_free_vgpr 192
		.amdhsa_next_free_sgpr 91
		.amdhsa_accum_offset 192
		.amdhsa_reserve_vcc 1
		.amdhsa_float_round_mode_32 0
		.amdhsa_float_round_mode_16_64 0
		.amdhsa_float_denorm_mode_32 3
		.amdhsa_float_denorm_mode_16_64 3
		.amdhsa_dx10_clamp 1
		.amdhsa_ieee_mode 1
		.amdhsa_fp16_overflow 0
		.amdhsa_tg_split 0
		.amdhsa_exception_fp_ieee_invalid_op 0
		.amdhsa_exception_fp_denorm_src 0
		.amdhsa_exception_fp_ieee_div_zero 0
		.amdhsa_exception_fp_ieee_overflow 0
		.amdhsa_exception_fp_ieee_underflow 0
		.amdhsa_exception_fp_ieee_inexact 0
		.amdhsa_exception_int_div_zero 0
	.end_amdhsa_kernel

amdhsa.kernels:
  - .agpr_count:     0
    .args:
      - .actual_access:  read_only
        .address_space:  global
        .offset:         0
        .size:           8
        .value_kind:     global_buffer
      - .actual_access:  read_only
        .address_space:  global
        .offset:         8
        .size:           8
        .value_kind:     global_buffer
      - .actual_access:  read_only
        .address_space:  global
        .offset:         16
        .size:           8
        .value_kind:     global_buffer
      - .actual_access:  read_only
        .address_space:  global
        .offset:         24
        .size:           8
        .value_kind:     global_buffer
      - .actual_access:  read_only
        .address_space:  global
        .offset:         32
        .size:           8
        .value_kind:     global_buffer
      - .actual_access:  read_only
        .address_space:  global
        .offset:         40
        .size:           8
        .value_kind:     global_buffer
      - .actual_access:  read_only
        .address_space:  global
        .offset:         48
        .size:           8
        .value_kind:     global_buffer
      - .actual_access:  read_only
        .address_space:  global
        .offset:         56
        .size:           8
        .value_kind:     global_buffer
      - .actual_access:  read_only
        .address_space:  global
        .offset:         64
        .size:           8
        .value_kind:     global_buffer
      - .actual_access:  read_only
        .address_space:  global
        .offset:         72
        .size:           8
        .value_kind:     global_buffer
      - .actual_access:  write_only
        .address_space:  global
        .offset:         80
        .size:           8
        .value_kind:     global_buffer
    .group_segment_fixed_size: 13056
    .kernarg_segment_align: 8
    .kernarg_segment_size: 88
    .language:       OpenCL C
    .language_version:
      - 2
      - 0
    .max_flat_workgroup_size: 128
    .name:           _Z11prep_kernelPKfS0_PKiS2_S0_S0_S0_S0_S0_S0_Pc
    .private_segment_fixed_size: 0
    .sgpr_count:     38
    .sgpr_spill_count: 0
    .symbol:         _Z11prep_kernelPKfS0_PKiS2_S0_S0_S0_S0_S0_S0_Pc.kd
    .uniform_work_group_size: 1
    .uses_dynamic_stack: false
    .vgpr_count:     192
    .vgpr_spill_count: 0
    .wavefront_size: 64
  - .agpr_count:     0
    .args:
      - .actual_access:  read_only
        .address_space:  global
        .offset:         0
        .size:           8
        .value_kind:     global_buffer
      - .actual_access:  read_only
        .address_space:  global
        .offset:         8
        .size:           8
        .value_kind:     global_buffer
      - .actual_access:  read_only
        .address_space:  global
        .offset:         16
        .size:           8
        .value_kind:     global_buffer
      - .actual_access:  read_only
        .address_space:  global
        .offset:         24
        .size:           8
        .value_kind:     global_buffer
      - .actual_access:  read_only
        .address_space:  global
        .offset:         32
        .size:           8
        .value_kind:     global_buffer
      - .actual_access:  read_only
        .address_space:  global
        .offset:         40
        .size:           8
        .value_kind:     global_buffer
      - .actual_access:  read_only
        .address_space:  global
        .offset:         48
        .size:           8
        .value_kind:     global_buffer
      - .actual_access:  write_only
        .address_space:  global
        .offset:         56
        .size:           8
        .value_kind:     global_buffer
    .group_segment_fixed_size: 16640
    .kernarg_segment_align: 8
    .kernarg_segment_size: 64
    .language:       OpenCL C
    .language_version:
      - 2
      - 0
    .max_flat_workgroup_size: 256
    .name:           _Z11attn_kernelILi4EEvPKfS1_S1_S1_S1_S1_PKcPf
    .private_segment_fixed_size: 0
    .sgpr_count:     38
    .sgpr_spill_count: 0
    .symbol:         _Z11attn_kernelILi4EEvPKfS1_S1_S1_S1_S1_PKcPf.kd
    .uniform_work_group_size: 1
    .uses_dynamic_stack: false
    .vgpr_count:     256
    .vgpr_spill_count: 0
    .wavefront_size: 64
